# union10 + the two remaining K-loop relax branches (third phase of the out and up GEMMs) inverted the same way: common path falls through
# baseline (speedup 1.0000x reference)
; #define PG8_STAGE(bufoff, gbase, voff) do { _Pragma("unroll") for (int _i = 0; _i < 2; ++_i) \
;         __builtin_amdgcn_global_load_lds((const unsigned*)((const char*)(gbase) + (voff)[_i]), (PG8_LAS unsigned*)(lds + (bufoff) + ldsw + _i * 8192), 16, 0, 0); } while (0)
; #define PG8_LDA(dst, b, h) do { _Pragma("unroll") for (int m = 0; m < 4; ++m) _Pragma("unroll") for (int k = 0; k < 2; ++k) dst[m][k] = *(const PG8_LAS bf16x8*)(lds + PG8_SA(b, h) + aoff + m * 2048 + k * 1024); } while (0)
; #define PG8_LDB(dst, b, h) do { _Pragma("unroll") for (int n = 0; n < 2; ++n) _Pragma("unroll") for (int k = 0; k < 2; ++k) dst[n][k] = *(const PG8_LAS bf16x8*)(lds + PG8_SB(b, h) + boff + n * 2048 + k * 1024); } while (0)
; #define PG8_MMA(ai, bj, At, Bt) do { __builtin_amdgcn_s_setprio(1); _Pragma("unroll") for (int m = 0; m < 4; ++m) _Pragma("unroll") for (int n = 0; n < 2; ++n) _Pragma("unroll") for (int k = 0; k < 2; ++k) \
;         acc[ai][bj][m][n] = mma16(Bt[n][k], At[m][k], acc[ai][bj][m][n]); __builtin_amdgcn_s_setprio(0); } while (0)
; #define PG8_WAIT_V(n) asm volatile("s_waitcnt vmcnt(" #n ")" ::: "memory")
; #define PG8_WAIT_VN(n) asm volatile("s_waitcnt vmcnt(%0)" :: "n"(n) : "memory")
; #define PG8_WAIT_L(n) asm volatile("s_waitcnt lgkmcnt(" #n ")" ::: "memory")
; #define PG8_BAR __builtin_amdgcn_s_barrier()
; #define PG8_SCHED __builtin_amdgcn_sched_barrier(0)
; template <class Epi, class Sched, bool ALIGN_EPI = false, bool SP2 = false>
; __device__ __forceinline__ void gemm_phase(PG8_LAS unsigned char* lds, const Gemm g, const Sched& S, const Epi& E, Stopwatch& sw) {
;     ...
;             if (relax) PG8_WAIT_VN(8 + Epi::NST); else PG8_WAIT_V(8); PG8_WAIT_L(0); PG8_BAR; PG8_MMA(1, 0, At, B0); PG8_MMA(1, 1, At, B1); PG8_BAR; PG8_SCHED;
;             PG8_LDB(B0, 1, 0); PG8_LDB(B1, 1, 1); PG8_SCHED; PG8_LDA(At, 1, 0); PG8_STAGE(PG8_SA(0, 1), a2 + hstep, voffA);
;             if (relax) PG8_WAIT_VN(8 + Epi::NST); else PG8_WAIT_V(8); PG8_WAIT_L(0); PG8_BAR; PG8_MMA(0, 0, At, B0); PG8_MMA(0, 1, At, B1); PG8_BAR; PG8_SCHED;
.LBB0_896:
	s_waitcnt lgkmcnt(0)
	s_barrier
	s_setprio 1
	s_waitcnt lgkmcnt(0)
	v_mfma_f32_16x16x32_bf16 v[64:67], v[148:151], v[188:191], v[64:67]
	v_mfma_f32_16x16x32_bf16 v[60:63], v[156:159], v[188:191], v[60:63]
	v_mfma_f32_16x16x32_bf16 v[48:51], v[148:151], v[180:183], v[48:51]
	v_mfma_f32_16x16x32_bf16 v[44:47], v[156:159], v[180:183], v[44:47]
	v_mfma_f32_16x16x32_bf16 v[32:35], v[148:151], v[172:175], v[32:35]
	v_mfma_f32_16x16x32_bf16 v[28:31], v[156:159], v[172:175], v[28:31]
	v_mfma_f32_16x16x32_bf16 v[16:19], v[148:151], v[164:167], v[16:19]
	v_mfma_f32_16x16x32_bf16 v[12:15], v[156:159], v[164:167], v[12:15]
	v_mfma_f32_16x16x32_bf16 v[64:67], v[152:155], v[192:195], v[64:67]
	v_mfma_f32_16x16x32_bf16 v[60:63], v[160:163], v[192:195], v[60:63]
	v_mfma_f32_16x16x32_bf16 v[48:51], v[152:155], v[184:187], v[48:51]
	v_mfma_f32_16x16x32_bf16 v[44:47], v[160:163], v[184:187], v[44:47]
	v_mfma_f32_16x16x32_bf16 v[32:35], v[152:155], v[176:179], v[32:35]
	v_mfma_f32_16x16x32_bf16 v[28:31], v[160:163], v[176:179], v[28:31]
	v_mfma_f32_16x16x32_bf16 v[16:19], v[152:155], v[168:171], v[16:19]
	v_mfma_f32_16x16x32_bf16 v[12:15], v[160:163], v[168:171], v[12:15]
	v_mfma_f32_16x16x32_bf16 v[56:59], v[132:135], v[188:191], v[56:59]
	v_mfma_f32_16x16x32_bf16 v[52:55], v[140:143], v[188:191], v[52:55]
	v_mfma_f32_16x16x32_bf16 v[40:43], v[132:135], v[180:183], v[40:43]
	v_mfma_f32_16x16x32_bf16 v[36:39], v[140:143], v[180:183], v[36:39]
	v_mfma_f32_16x16x32_bf16 v[24:27], v[132:135], v[172:175], v[24:27]
	v_mfma_f32_16x16x32_bf16 v[20:23], v[140:143], v[172:175], v[20:23]
	v_mfma_f32_16x16x32_bf16 v[8:11], v[132:135], v[164:167], v[8:11]
	v_mfma_f32_16x16x32_bf16 v[4:7], v[140:143], v[164:167], v[4:7]
	v_mfma_f32_16x16x32_bf16 v[56:59], v[136:139], v[192:195], v[56:59]
	v_mfma_f32_16x16x32_bf16 v[52:55], v[144:147], v[192:195], v[52:55]
	v_mfma_f32_16x16x32_bf16 v[40:43], v[136:139], v[184:187], v[40:43]
	v_mfma_f32_16x16x32_bf16 v[36:39], v[144:147], v[184:187], v[36:39]
	v_mfma_f32_16x16x32_bf16 v[24:27], v[136:139], v[176:179], v[24:27]
	v_mfma_f32_16x16x32_bf16 v[20:23], v[144:147], v[176:179], v[20:23]
	v_mfma_f32_16x16x32_bf16 v[8:11], v[136:139], v[168:171], v[8:11]
	v_mfma_f32_16x16x32_bf16 v[4:7], v[144:147], v[168:171], v[4:7]
	s_setprio 0
	s_barrier
	v_add_u32_e32 v132, 0x18000, v227
	v_add_u32_e32 v144, 0x1c000, v227
	ds_read_b128 v[148:151], v132
	ds_read_b128 v[152:155], v132 offset:1024
	ds_read_b128 v[156:159], v132 offset:2048
	ds_read_b128 v[160:163], v132 offset:3072
	ds_read_b128 v[132:135], v144
	ds_read_b128 v[136:139], v144 offset:1024
	ds_read_b128 v[140:143], v144 offset:2048
	ds_read_b128 v[144:147], v144 offset:3072
	s_add_u32 s74, s74, 0x80000
	s_addc_u32 s75, s75, 0
	s_mov_b32 m0, s36
	v_lshl_add_u64 v[230:231], s[74:75], 0, v[204:205]
	ds_read_b128 v[188:191], v228 offset:32768
	ds_read_b128 v[192:195], v228 offset:33792
	ds_read_b128 v[180:183], v228 offset:34816
	ds_read_b128 v[184:187], v228 offset:35840
	ds_read_b128 v[172:175], v228 offset:36864
	ds_read_b128 v[176:179], v228 offset:37888
	ds_read_b128 v[164:167], v228 offset:38912
	ds_read_b128 v[168:171], v228 offset:39936
	global_load_lds_dwordx4 v[230:231], off
	v_lshl_add_u64 v[230:231], s[74:75], 0, v[202:203]
	s_mov_b32 m0, s37
	s_and_b64 vcc, exec, s[42:43]
	global_load_lds_dwordx4 v[230:231], off
	s_cbranch_vccz .Lrlx_b0
	s_mov_b64 s[74:75], s[10:11]

; #define PG8_STAGE(bufoff, gbase, voff) do { _Pragma("unroll") for (int _i = 0; _i < 2; ++_i) \
;         __builtin_amdgcn_global_load_lds((const unsigned*)((const char*)(gbase) + (voff)[_i]), (PG8_LAS unsigned*)(lds + (bufoff) + ldsw + _i * 8192), 16, 0, 0); } while (0)
; #define PG8_LDA(dst, b, h) do { _Pragma("unroll") for (int m = 0; m < 4; ++m) _Pragma("unroll") for (int k = 0; k < 2; ++k) dst[m][k] = *(const PG8_LAS bf16x8*)(lds + PG8_SA(b, h) + aoff + m * 2048 + k * 1024); } while (0)
; #define PG8_LDB(dst, b, h) do { _Pragma("unroll") for (int n = 0; n < 2; ++n) _Pragma("unroll") for (int k = 0; k < 2; ++k) dst[n][k] = *(const PG8_LAS bf16x8*)(lds + PG8_SB(b, h) + boff + n * 2048 + k * 1024); } while (0)
; #define PG8_MMA(ai, bj, At, Bt) do { __builtin_amdgcn_s_setprio(1); _Pragma("unroll") for (int m = 0; m < 4; ++m) _Pragma("unroll") for (int n = 0; n < 2; ++n) _Pragma("unroll") for (int k = 0; k < 2; ++k) \
;         acc[ai][bj][m][n] = mma16(Bt[n][k], At[m][k], acc[ai][bj][m][n]); __builtin_amdgcn_s_setprio(0); } while (0)
; #define PG8_WAIT_V(n) asm volatile("s_waitcnt vmcnt(" #n ")" ::: "memory")
; #define PG8_WAIT_VN(n) asm volatile("s_waitcnt vmcnt(%0)" :: "n"(n) : "memory")
; #define PG8_WAIT_L(n) asm volatile("s_waitcnt lgkmcnt(" #n ")" ::: "memory")
; #define PG8_BAR __builtin_amdgcn_s_barrier()
; #define PG8_SCHED __builtin_amdgcn_sched_barrier(0)
; template <class Epi, class Sched, bool ALIGN_EPI = false, bool SP2 = false>
; __device__ __forceinline__ void gemm_phase(PG8_LAS unsigned char* lds, const Gemm g, const Sched& S, const Epi& E, Stopwatch& sw) {
;     ...
;             PG8_LDB(B0, 1, 0); PG8_LDB(B1, 1, 1); PG8_SCHED; PG8_LDA(At, 1, 0); PG8_STAGE(PG8_SA(0, 1), a2 + hstep, voffA);
;             if (relax) PG8_WAIT_VN(8 + Epi::NST); else PG8_WAIT_V(8); PG8_WAIT_L(0); PG8_BAR; PG8_MMA(0, 0, At, B0); PG8_MMA(0, 1, At, B1); PG8_BAR; PG8_SCHED;
.Lrlx_b0:
	s_waitcnt vmcnt(32)
	s_mov_b64 s[74:75], s[10:11]
	s_branch .LBB0_899

; #define PG8_STAGE(bufoff, gbase, voff) do { _Pragma("unroll") for (int _i = 0; _i < 2; ++_i) \
;         __builtin_amdgcn_global_load_lds((const unsigned*)((const char*)(gbase) + (voff)[_i]), (PG8_LAS unsigned*)(lds + (bufoff) + ldsw + _i * 8192), 16, 0, 0); } while (0)
; #define PG8_LDA(dst, b, h) do { _Pragma("unroll") for (int m = 0; m < 4; ++m) _Pragma("unroll") for (int k = 0; k < 2; ++k) dst[m][k] = *(const PG8_LAS bf16x8*)(lds + PG8_SA(b, h) + aoff + m * 2048 + k * 1024); } while (0)
; #define PG8_LDB(dst, b, h) do { _Pragma("unroll") for (int n = 0; n < 2; ++n) _Pragma("unroll") for (int k = 0; k < 2; ++k) dst[n][k] = *(const PG8_LAS bf16x8*)(lds + PG8_SB(b, h) + boff + n * 2048 + k * 1024); } while (0)
; #define PG8_MMA(ai, bj, At, Bt) do { __builtin_amdgcn_s_setprio(1); _Pragma("unroll") for (int m = 0; m < 4; ++m) _Pragma("unroll") for (int n = 0; n < 2; ++n) _Pragma("unroll") for (int k = 0; k < 2; ++k) \
;         acc[ai][bj][m][n] = mma16(Bt[n][k], At[m][k], acc[ai][bj][m][n]); __builtin_amdgcn_s_setprio(0); } while (0)
; #define PG8_WAIT_V(n) asm volatile("s_waitcnt vmcnt(" #n ")" ::: "memory")
; #define PG8_WAIT_VN(n) asm volatile("s_waitcnt vmcnt(%0)" :: "n"(n) : "memory")
; #define PG8_WAIT_L(n) asm volatile("s_waitcnt lgkmcnt(" #n ")" ::: "memory")
; #define PG8_BAR __builtin_amdgcn_s_barrier()
; #define PG8_SCHED __builtin_amdgcn_sched_barrier(0)
; template <class Epi, class Sched, bool ALIGN_EPI = false, bool SP2 = false>
; __device__ __forceinline__ void gemm_phase(PG8_LAS unsigned char* lds, const Gemm g, const Sched& S, const Epi& E, Stopwatch& sw) {
;     ...
;             if (relax) PG8_WAIT_VN(8 + Epi::NST); else PG8_WAIT_V(8); PG8_WAIT_L(0); PG8_BAR; PG8_MMA(1, 0, At, B0); PG8_MMA(1, 1, At, B1); PG8_BAR; PG8_SCHED;
;             PG8_LDB(B0, 1, 0); PG8_LDB(B1, 1, 1); PG8_SCHED; PG8_LDA(At, 1, 0); PG8_STAGE(PG8_SA(0, 1), a2 + hstep, voffA);
;             if (relax) PG8_WAIT_VN(8 + Epi::NST); else PG8_WAIT_V(8); PG8_WAIT_L(0); PG8_BAR; PG8_MMA(0, 0, At, B0); PG8_MMA(0, 1, At, B1); PG8_BAR; PG8_SCHED;
.LBB0_1124:
	s_waitcnt lgkmcnt(0)
	s_barrier
	s_setprio 1
	s_waitcnt lgkmcnt(0)
	v_mfma_i32_16x16x64_i8 v[96:99], v[148:151], v[188:191], v[96:99]
	v_mfma_i32_16x16x64_i8 v[92:95], v[156:159], v[188:191], v[92:95]
	v_mfma_i32_16x16x64_i8 v[88:91], v[148:151], v[180:183], v[88:91]
	v_mfma_i32_16x16x64_i8 v[84:87], v[156:159], v[180:183], v[84:87]
	v_mfma_i32_16x16x64_i8 v[80:83], v[148:151], v[172:175], v[80:83]
	v_mfma_i32_16x16x64_i8 v[72:75], v[156:159], v[172:175], v[72:75]
	v_mfma_i32_16x16x64_i8 v[64:67], v[148:151], v[164:167], v[64:67]
	v_mfma_i32_16x16x64_i8 v[56:59], v[156:159], v[164:167], v[56:59]
	v_mfma_i32_16x16x64_i8 v[96:99], v[152:155], v[192:195], v[96:99]
	v_mfma_i32_16x16x64_i8 v[92:95], v[160:163], v[192:195], v[92:95]
	v_mfma_i32_16x16x64_i8 v[88:91], v[152:155], v[184:187], v[88:91]
	v_mfma_i32_16x16x64_i8 v[84:87], v[160:163], v[184:187], v[84:87]
	v_mfma_i32_16x16x64_i8 v[80:83], v[152:155], v[176:179], v[80:83]
	v_mfma_i32_16x16x64_i8 v[72:75], v[160:163], v[176:179], v[72:75]
	v_mfma_i32_16x16x64_i8 v[64:67], v[152:155], v[168:171], v[64:67]
	v_mfma_i32_16x16x64_i8 v[56:59], v[160:163], v[168:171], v[56:59]
	v_mfma_i32_16x16x64_i8 v[32:35], v[132:135], v[188:191], v[32:35]
	v_mfma_i32_16x16x64_i8 v[28:31], v[140:143], v[188:191], v[28:31]
	v_mfma_i32_16x16x64_i8 v[24:27], v[132:135], v[180:183], v[24:27]
	v_mfma_i32_16x16x64_i8 v[20:23], v[140:143], v[180:183], v[20:23]
	v_mfma_i32_16x16x64_i8 v[16:19], v[132:135], v[172:175], v[16:19]
	v_mfma_i32_16x16x64_i8 v[12:15], v[140:143], v[172:175], v[12:15]
	v_mfma_i32_16x16x64_i8 v[8:11], v[132:135], v[164:167], v[8:11]
	v_mfma_i32_16x16x64_i8 v[4:7], v[140:143], v[164:167], v[4:7]
	v_mfma_i32_16x16x64_i8 v[32:35], v[136:139], v[192:195], v[32:35]
	v_mfma_i32_16x16x64_i8 v[28:31], v[144:147], v[192:195], v[28:31]
	v_mfma_i32_16x16x64_i8 v[24:27], v[136:139], v[184:187], v[24:27]
	v_mfma_i32_16x16x64_i8 v[20:23], v[144:147], v[184:187], v[20:23]
	v_mfma_i32_16x16x64_i8 v[16:19], v[136:139], v[176:179], v[16:19]
	v_mfma_i32_16x16x64_i8 v[12:15], v[144:147], v[176:179], v[12:15]
	v_mfma_i32_16x16x64_i8 v[8:11], v[136:139], v[168:171], v[8:11]
	v_mfma_i32_16x16x64_i8 v[4:7], v[144:147], v[168:171], v[4:7]
	s_setprio 0
	s_barrier
	v_add_u32_e32 v132, 0x18000, v227
	v_add_u32_e32 v144, 0x19000, v227
	ds_read_b128 v[148:151], v132
	ds_read_b128 v[152:155], v132 offset:1024
	ds_read_b128 v[156:159], v132 offset:2048
	ds_read_b128 v[160:163], v132 offset:3072
	ds_read_b128 v[132:135], v144
	ds_read_b128 v[136:139], v144 offset:1024
	ds_read_b128 v[140:143], v144 offset:2048
	ds_read_b128 v[144:147], v144 offset:3072
	s_add_u32 s74, s74, 0x40000
	s_addc_u32 s75, s75, 0
	s_mov_b32 m0, s80
	v_lshl_add_u64 v[230:231], s[74:75], 0, v[204:205]
	ds_read_b128 v[188:191], v228 offset:32768
	ds_read_b128 v[192:195], v228 offset:33792
	ds_read_b128 v[180:183], v228 offset:34816
	ds_read_b128 v[184:187], v228 offset:35840
	ds_read_b128 v[172:175], v228 offset:36864
	ds_read_b128 v[176:179], v228 offset:37888
	ds_read_b128 v[164:167], v228 offset:38912
	ds_read_b128 v[168:171], v228 offset:39936
	global_load_lds_dwordx4 v[230:231], off
	v_lshl_add_u64 v[230:231], s[74:75], 0, v[202:203]
	s_mov_b32 m0, s81
	s_and_b64 vcc, exec, s[40:41]
	global_load_lds_dwordx4 v[230:231], off
	s_cbranch_vccz .Lrlx_b1
	s_mov_b64 s[74:75], s[10:11]

; #define PG8_STAGE(bufoff, gbase, voff) do { _Pragma("unroll") for (int _i = 0; _i < 2; ++_i) \
;         __builtin_amdgcn_global_load_lds((const unsigned*)((const char*)(gbase) + (voff)[_i]), (PG8_LAS unsigned*)(lds + (bufoff) + ldsw + _i * 8192), 16, 0, 0); } while (0)
; #define PG8_LDA(dst, b, h) do { _Pragma("unroll") for (int m = 0; m < 4; ++m) _Pragma("unroll") for (int k = 0; k < 2; ++k) dst[m][k] = *(const PG8_LAS bf16x8*)(lds + PG8_SA(b, h) + aoff + m * 2048 + k * 1024); } while (0)
; #define PG8_LDB(dst, b, h) do { _Pragma("unroll") for (int n = 0; n < 2; ++n) _Pragma("unroll") for (int k = 0; k < 2; ++k) dst[n][k] = *(const PG8_LAS bf16x8*)(lds + PG8_SB(b, h) + boff + n * 2048 + k * 1024); } while (0)
; #define PG8_MMA(ai, bj, At, Bt) do { __builtin_amdgcn_s_setprio(1); _Pragma("unroll") for (int m = 0; m < 4; ++m) _Pragma("unroll") for (int n = 0; n < 2; ++n) _Pragma("unroll") for (int k = 0; k < 2; ++k) \
;         acc[ai][bj][m][n] = mma16(Bt[n][k], At[m][k], acc[ai][bj][m][n]); __builtin_amdgcn_s_setprio(0); } while (0)
; #define PG8_WAIT_V(n) asm volatile("s_waitcnt vmcnt(" #n ")" ::: "memory")
; #define PG8_WAIT_VN(n) asm volatile("s_waitcnt vmcnt(%0)" :: "n"(n) : "memory")
; #define PG8_WAIT_L(n) asm volatile("s_waitcnt lgkmcnt(" #n ")" ::: "memory")
; #define PG8_BAR __builtin_amdgcn_s_barrier()
; #define PG8_SCHED __builtin_amdgcn_sched_barrier(0)
; template <class Epi, class Sched, bool ALIGN_EPI = false, bool SP2 = false>
; __device__ __forceinline__ void gemm_phase(PG8_LAS unsigned char* lds, const Gemm g, const Sched& S, const Epi& E, Stopwatch& sw) {
;     ...
;             PG8_LDB(B0, 1, 0); PG8_LDB(B1, 1, 1); PG8_SCHED; PG8_LDA(At, 1, 0); PG8_STAGE(PG8_SA(0, 1), a2 + hstep, voffA);
;             if (relax) PG8_WAIT_VN(8 + Epi::NST); else PG8_WAIT_V(8); PG8_WAIT_L(0); PG8_BAR; PG8_MMA(0, 0, At, B0); PG8_MMA(0, 1, At, B1); PG8_BAR; PG8_SCHED;
.Lrlx_b1:
	s_waitcnt vmcnt(24)
	s_mov_b64 s[74:75], s[10:11]
	s_branch .LBB0_1127
